# P6: stores transposed within 8-lane groups so each store instruction writes full 128-byte lines (was 64-byte quads)
# speedup vs baseline: 1.0010x; 1.0010x over previous
; __device__ __forceinline__ int otid() { int t = threadIdx.x; asm volatile("" : "+v"(t)); return t; }
; __device__ void phase6(const Params& p) {
;     const int tid_ = otid(); const int lane = tid_ & 63, wid = tid_ >> 6;
;     const int nw = gridDim.x * NWV;
;     int R = blockIdx.x * NWV + wid;
;     if (R >= NLAT) return;
;     uint4 ywn[8], xan, xbn, san, sbn; float4 gan, gbn;
;     ...
;     P6_LOAD(R);
;     int bcur = -1; float4 g2v[4];
;     for (;;) {
;         uint4 yw[8]; const uint4 xa = xan, xb = xbn, sa = san, sb = sbn; const float4 ga = gan, gb = gbn;
; #pragma unroll
;         for (int k = 0; k < 8; ++k) yw[k] = ywn[k];
;         const int Rn = R + nw; const bool more = Rn < NLAT;
;         if (more) P6_LOAD(Rn);
;         const int b = R >> 13;
;         if (b != bcur) { bcur = b;
; #pragma unroll
;             for (int q = 0; q < 4; ++q) g2v[q] = *(const float4*)(p.mod + b * 6144 + 5120 + lane * 16 + q * 4); }
;         const float gk[8] = {ga.x * 0.0625f, ga.y * 0.0625f, ga.z * 0.0625f, ga.w * 0.0625f, gb.x * 0.0625f, gb.y * 0.0625f, gb.z * 0.0625f, gb.w * 0.0625f};
;         float sacc[16];
; #pragma unroll
;         for (int j = 0; j < 16; ++j) sacc[j] = 0.f;
; #pragma unroll
;         for (int k = 0; k < 8; ++k) {
;             const unsigned wv[4] = {yw[k].x, yw[k].y, yw[k].z, yw[k].w};
; #pragma unroll
;             for (int q = 0; q < 4; ++q) {
;                 const f32v2 lo = __builtin_amdgcn_cvt_pk_f32_fp8((int)wv[q], false), hi = __builtin_amdgcn_cvt_pk_f32_fp8((int)wv[q], true);
;                 sacc[q * 4 + 0] += gk[k] * lo[0]; sacc[q * 4 + 1] += gk[k] * lo[1]; sacc[q * 4 + 2] += gk[k] * hi[0]; sacc[q * 4 + 3] += gk[k] * hi[1];
.LBB0_1289:
	s_or_b64 exec, exec, s[0:1]
	s_waitcnt lgkmcnt(0)
	s_barrier
	v_lshlrev_b32_e32 v246, 6, v0
	v_and_b32_e32 v247, 7, v0
	v_mul_u32_u24_e32 v252, 48, v247
	v_sub_u32_e32 v247, v246, v252
	v_sub_u32_e32 v252, 0, v252
	v_ashrrev_i32_e32 v253, 31, v252
	s_mov_b32 s22, 0x8000
	v_ashrrev_i32_e32 v1, 6, v0
	v_add_u32_e32 v138, s81, v1
	v_cmp_gt_i32_e32 vcc, s22, v138
	s_and_saveexec_b64 s[0:1], vcc
	s_cbranch_execz .LBB0_1296
	v_ashrrev_i32_e32 v139, 31, v138
	v_lshlrev_b64 v[2:3], 13, v[138:139]
	v_lshlrev_b32_e32 v1, 4, v0
	v_lshl_add_u64 v[2:3], s[50:51], 0, v[2:3]
	v_and_b32_e32 v130, 0x3f0, v1
	v_mov_b32_e32 v131, 0
	v_lshl_add_u64 v[2:3], v[2:3], 0, v[130:131]
	s_movk_i32 s0, 0x1000
	global_load_dwordx4 v[62:65], v[2:3], off
	global_load_dwordx4 v[58:61], v[2:3], off offset:1024
	global_load_dwordx4 v[54:57], v[2:3], off offset:2048
	global_load_dwordx4 v[46:49], v[2:3], off offset:3072
	v_add_co_u32_e32 v2, vcc, s0, v2
	v_lshlrev_b64 v[6:7], 11, v[138:139]
	s_nop 0
	v_addc_co_u32_e32 v3, vcc, 0, v3, vcc
	global_load_dwordx4 v[50:53], v[2:3], off
	global_load_dwordx4 v[42:45], v[2:3], off offset:1024
	global_load_dwordx4 v[38:41], v[2:3], off offset:2048
	global_load_dwordx4 v[34:37], v[2:3], off offset:3072
	v_lshl_add_u64 v[2:3], s[24:25], 0, v[6:7]
	v_lshlrev_b32_e32 v8, 1, v130
	v_mov_b32_e32 v9, v131
	v_lshl_add_u64 v[10:11], v[2:3], 0, v[8:9]
	v_lshl_add_u64 v[6:7], s[26:27], 0, v[6:7]
	global_load_dwordx4 v[2:5], v[10:11], off offset:16
	global_load_dwordx4 v[26:29], v[10:11], off
	v_lshl_add_u64 v[10:11], v[6:7], 0, v[8:9]
	global_load_dwordx4 v[6:9], v[10:11], off offset:16
	global_load_dwordx4 v[30:33], v[10:11], off
	v_lshlrev_b64 v[10:11], 5, v[138:139]
	v_lshl_add_u64 v[10:11], s[36:37], 0, v[10:11]
	global_load_dwordx4 v[114:117], v[10:11], off offset:16
	global_load_dwordx4 v[118:121], v[10:11], off
	v_lshlrev_b64 v[10:11], 12, v[138:139]
	v_and_b32_e32 v12, 63, v0
	v_lshl_or_b32 v10, v12, 6, v10
	v_lshl_add_u64 v[0:1], s[88:89], 0, v[10:11]
	v_add_u32_e32 v10, s82, v138
	v_ashrrev_i32_e32 v11, 31, v10
	s_ashr_i32 s83, s82, 31
	v_lshlrev_b64 v[134:135], 11, v[10:11]
	v_lshlrev_b64 v[136:137], 13, v[10:11]
	s_lshl_b64 s[2:3], s[82:83], 12
	v_lshlrev_b64 v[132:133], 5, v[10:11]
	s_lshl_b64 s[4:5], s[82:83], 5
	v_lshl_or_b32 v134, v12, 5, v134
	s_lshl_b64 s[6:7], s[82:83], 11
	v_or_b32_e32 v136, v136, v130
	s_lshl_b64 s[8:9], s[82:83], 13
	v_mov_b32_e32 v139, -1
	s_mov_b64 s[10:11], 0
	s_movk_i32 s23, 0x7fff
	s_mov_b32 s24, 0x17de8000
	s_mov_b32 s25, 0x17de9000
	s_mov_b64 s[12:13], 0x13de7600
	s_mov_b32 s26, 0x13de7000
	s_mov_b64 s[14:15], 0xce7600
	s_mov_b32 s27, 0xce7000
	s_mov_b64 s[16:17], 0x4ce7600
	v_lshlrev_b32_e32 v130, 2, v130
	s_mov_b64 s[18:19], 0x5000
	s_branch .LBB0_1292
.LBB0_1291:
	s_or_b64 exec, exec, s[20:21]
	v_cvt_pk_f32_fp8_e32 v[146:147], v62
	v_cvt_pk_f32_fp8_e32 v[158:159], v58
	v_cvt_pk_f32_fp8_e32 v[170:171], v54
	v_mul_f32_e32 v118, 0x3d800000, v118
	v_cvt_pk_f32_fp8_e32 v[182:183], v46
	v_mul_f32_e32 v138, 0x3d800000, v119
	v_cvt_pk_f32_fp8_e32 v[194:195], v50
	v_pk_fma_f32 v[146:147], v[118:119], v[146:147], 0 op_sel_hi:[0,1,0]
	v_mul_f32_e32 v120, 0x3d800000, v120
	v_cvt_pk_f32_fp8_e32 v[206:207], v42
	v_pk_fma_f32 v[146:147], v[138:139], v[158:159], v[146:147] op_sel_hi:[0,1,1]
	v_mul_f32_e32 v140, 0x3d800000, v121
	v_cvt_pk_f32_fp8_e32 v[218:219], v38
	v_pk_fma_f32 v[146:147], v[120:121], v[170:171], v[146:147] op_sel_hi:[0,1,1]
	v_mul_f32_e32 v114, 0x3d800000, v114
	v_cvt_pk_f32_fp8_e32 v[230:231], v34
	v_pk_fma_f32 v[146:147], v[140:141], v[182:183], v[146:147] op_sel_hi:[0,1,1]
	v_mul_f32_e32 v142, 0x3d800000, v115
	v_pk_fma_f32 v[146:147], v[114:115], v[194:195], v[146:147] op_sel_hi:[0,1,1]
	v_mul_f32_e32 v116, 0x3d800000, v116
	v_cvt_pk_f32_fp8_sdwa v[148:149], v62 src0_sel:WORD_1
	v_pk_fma_f32 v[146:147], v[142:143], v[206:207], v[146:147] op_sel_hi:[0,1,1]
	v_mul_f32_e32 v144, 0x3d800000, v117
	v_cvt_pk_f32_fp8_sdwa v[160:161], v58 src0_sel:WORD_1
	v_pk_fma_f32 v[146:147], v[116:117], v[218:219], v[146:147] op_sel_hi:[0,1,1]
	v_cvt_pk_f32_fp8_sdwa v[172:173], v54 src0_sel:WORD_1
	v_cvt_pk_f32_fp8_e32 v[238:239], v36
	v_cvt_pk_f32_fp8_sdwa v[240:241], v36 src0_sel:WORD_1
	v_cvt_pk_f32_fp8_e32 v[242:243], v37
	v_cvt_pk_f32_fp8_sdwa v[244:245], v37 src0_sel:WORD_1
	v_lshlrev_b32_e32 v36, 16, v30
	v_and_b32_e32 v37, 0xffff0000, v30
	v_pk_fma_f32 v[146:147], v[144:145], v[230:231], v[146:147] op_sel_hi:[0,1,1]
	v_cvt_pk_f32_fp8_sdwa v[184:185], v46 src0_sel:WORD_1
	v_cvt_pk_f32_fp8_sdwa v[232:233], v34 src0_sel:WORD_1
	v_cvt_pk_f32_fp8_e32 v[234:235], v35
	v_cvt_pk_f32_fp8_sdwa v[236:237], v35 src0_sel:WORD_1
	v_lshlrev_b32_e32 v34, 16, v26
	v_and_b32_e32 v35, 0xffff0000, v26
	v_pk_add_f32 v[36:37], v[146:147], v[36:37]
	v_cvt_pk_f32_fp8_sdwa v[196:197], v50 src0_sel:WORD_1
	s_waitcnt vmcnt(3)
; __device__ void phase6(const Params& p) {
;     ...
;         for (int k = 0; k < 8; ++k) {
;             const unsigned wv[4] = {yw[k].x, yw[k].y, yw[k].z, yw[k].w};
; #pragma unroll
;             for (int q = 0; q < 4; ++q) {
;                 const f32v2 lo = __builtin_amdgcn_cvt_pk_f32_fp8((int)wv[q], false), hi = __builtin_amdgcn_cvt_pk_f32_fp8((int)wv[q], true);
;                 sacc[q * 4 + 0] += gk[k] * lo[0]; sacc[q * 4 + 1] += gk[k] * lo[1]; sacc[q * 4 + 2] += gk[k] * hi[0]; sacc[q * 4 + 3] += gk[k] * hi[1];
;             }
;         }
;         const unsigned xw[8] = {xa.x, xa.y, xa.z, xa.w, xb.x, xb.y, xb.z, xb.w}, sw[8] = {sa.x, sa.y, sa.z, sa.w, sb.x, sb.y, sb.z, sb.w};
; #pragma unroll
;         for (int q = 0; q < 4; ++q) {
;             const int col = lane * 16 + q * 4;
;             const float4 g2 = g2v[q];
;             float4 r;
;             r.x = __uint_as_float(xw[q * 2] << 16) + g2.x * (sacc[q * 4 + 0] + __uint_as_float(sw[q * 2] << 16));
;             r.y = __uint_as_float(xw[q * 2] & 0xffff0000u) + g2.y * (sacc[q * 4 + 1] + __uint_as_float(sw[q * 2] & 0xffff0000u));
;             r.z = __uint_as_float(xw[q * 2 + 1] << 16) + g2.z * (sacc[q * 4 + 2] + __uint_as_float(sw[q * 2 + 1] << 16));
;             r.w = __uint_as_float(xw[q * 2 + 1] & 0xffff0000u) + g2.w * (sacc[q * 4 + 3] + __uint_as_float(sw[q * 2 + 1] & 0xffff0000u));
;             *(float4*)(p.out + (size_t)R * D + col) = r;
	v_pk_fma_f32 v[34:35], v[10:11], v[36:37], v[34:35]
	v_pk_fma_f32 v[36:37], v[118:119], v[148:149], 0 op_sel_hi:[0,1,0]
	v_cvt_pk_f32_fp8_sdwa v[208:209], v42 src0_sel:WORD_1
	v_pk_fma_f32 v[36:37], v[138:139], v[160:161], v[36:37] op_sel_hi:[0,1,1]
	v_cvt_pk_f32_fp8_sdwa v[220:221], v38 src0_sel:WORD_1
	v_pk_fma_f32 v[36:37], v[120:121], v[172:173], v[36:37] op_sel_hi:[0,1,1]
	v_pk_fma_f32 v[36:37], v[140:141], v[184:185], v[36:37] op_sel_hi:[0,1,1]
	v_pk_fma_f32 v[36:37], v[114:115], v[196:197], v[36:37] op_sel_hi:[0,1,1]
	v_pk_fma_f32 v[36:37], v[142:143], v[208:209], v[36:37] op_sel_hi:[0,1,1]
	v_cvt_pk_f32_fp8_e32 v[150:151], v63
	v_pk_fma_f32 v[36:37], v[116:117], v[220:221], v[36:37] op_sel_hi:[0,1,1]
	v_cvt_pk_f32_fp8_e32 v[162:163], v59
	v_lshlrev_b32_e32 v30, 16, v31
	v_and_b32_e32 v31, 0xffff0000, v31
	v_pk_fma_f32 v[36:37], v[144:145], v[232:233], v[36:37] op_sel_hi:[0,1,1]
	v_cvt_pk_f32_fp8_e32 v[174:175], v55
	v_lshlrev_b32_e32 v26, 16, v27
	v_and_b32_e32 v27, 0xffff0000, v27
	v_pk_add_f32 v[30:31], v[36:37], v[30:31]
	v_cvt_pk_f32_fp8_e32 v[186:187], v47
	v_pk_fma_f32 v[36:37], v[12:13], v[30:31], v[26:27]
	v_cvt_pk_f32_fp8_e32 v[198:199], v51
	ds_write_b128 v246, v[34:37]
	v_cvt_pk_f32_fp8_e32 v[210:211], v43
	v_cvt_pk_f32_fp8_e32 v[222:223], v39
	v_pk_fma_f32 v[34:35], v[118:119], v[150:151], 0 op_sel_hi:[0,1,0]
	v_pk_fma_f32 v[34:35], v[138:139], v[162:163], v[34:35] op_sel_hi:[0,1,1]
	v_pk_fma_f32 v[34:35], v[120:121], v[174:175], v[34:35] op_sel_hi:[0,1,1]
	v_pk_fma_f32 v[34:35], v[140:141], v[186:187], v[34:35] op_sel_hi:[0,1,1]
	v_pk_fma_f32 v[34:35], v[114:115], v[198:199], v[34:35] op_sel_hi:[0,1,1]
	v_cvt_pk_f32_fp8_sdwa v[62:63], v63 src0_sel:WORD_1
	v_pk_fma_f32 v[34:35], v[142:143], v[210:211], v[34:35] op_sel_hi:[0,1,1]
	v_cvt_pk_f32_fp8_sdwa v[58:59], v59 src0_sel:WORD_1
	v_pk_fma_f32 v[34:35], v[116:117], v[222:223], v[34:35] op_sel_hi:[0,1,1]
	v_cvt_pk_f32_fp8_sdwa v[54:55], v55 src0_sel:WORD_1
	v_lshlrev_b32_e32 v30, 16, v32
	v_and_b32_e32 v31, 0xffff0000, v32
	v_pk_fma_f32 v[34:35], v[144:145], v[234:235], v[34:35] op_sel_hi:[0,1,1]
	v_cvt_pk_f32_fp8_sdwa v[46:47], v47 src0_sel:WORD_1
	v_lshlrev_b32_e32 v26, 16, v28
	v_and_b32_e32 v27, 0xffff0000, v28
	v_pk_add_f32 v[30:31], v[34:35], v[30:31]
	v_cvt_pk_f32_fp8_sdwa v[50:51], v51 src0_sel:WORD_1
	s_waitcnt vmcnt(0)
	v_pk_fma_f32 v[26:27], v[14:15], v[30:31], v[26:27]
	v_pk_fma_f32 v[30:31], v[118:119], v[62:63], 0 op_sel_hi:[0,1,0]
	v_cvt_pk_f32_fp8_sdwa v[42:43], v43 src0_sel:WORD_1
	v_pk_fma_f32 v[30:31], v[138:139], v[58:59], v[30:31] op_sel_hi:[0,1,1]
	v_cvt_pk_f32_fp8_sdwa v[38:39], v39 src0_sel:WORD_1
	v_pk_fma_f32 v[30:31], v[120:121], v[54:55], v[30:31] op_sel_hi:[0,1,1]
	v_pk_fma_f32 v[30:31], v[140:141], v[46:47], v[30:31] op_sel_hi:[0,1,1]
	v_pk_fma_f32 v[30:31], v[114:115], v[50:51], v[30:31] op_sel_hi:[0,1,1]
	v_cvt_pk_f32_fp8_e32 v[152:153], v64
	v_pk_fma_f32 v[30:31], v[142:143], v[42:43], v[30:31] op_sel_hi:[0,1,1]
	v_cvt_pk_f32_fp8_e32 v[164:165], v60
	v_pk_fma_f32 v[30:31], v[116:117], v[38:39], v[30:31] op_sel_hi:[0,1,1]
	v_cvt_pk_f32_fp8_e32 v[176:177], v56
	v_lshlrev_b32_e32 v32, 16, v33
	v_and_b32_e32 v33, 0xffff0000, v33
	v_pk_fma_f32 v[30:31], v[144:145], v[236:237], v[30:31] op_sel_hi:[0,1,1]
	v_cvt_pk_f32_fp8_e32 v[188:189], v48
	v_lshlrev_b32_e32 v28, 16, v29
	v_and_b32_e32 v29, 0xffff0000, v29
	v_pk_add_f32 v[30:31], v[30:31], v[32:33]
	v_cvt_pk_f32_fp8_e32 v[200:201], v52
	v_pk_fma_f32 v[28:29], v[16:17], v[30:31], v[28:29]
	v_pk_fma_f32 v[30:31], v[118:119], v[152:153], 0 op_sel_hi:[0,1,0]
	v_cvt_pk_f32_fp8_e32 v[212:213], v44
	v_pk_fma_f32 v[30:31], v[138:139], v[164:165], v[30:31] op_sel_hi:[0,1,1]
	v_cvt_pk_f32_fp8_e32 v[224:225], v40
	v_pk_fma_f32 v[30:31], v[120:121], v[176:177], v[30:31] op_sel_hi:[0,1,1]
	v_pk_fma_f32 v[30:31], v[140:141], v[188:189], v[30:31] op_sel_hi:[0,1,1]
	v_pk_fma_f32 v[30:31], v[114:115], v[200:201], v[30:31] op_sel_hi:[0,1,1]
	v_cvt_pk_f32_fp8_sdwa v[154:155], v64 src0_sel:WORD_1
	v_pk_fma_f32 v[30:31], v[142:143], v[212:213], v[30:31] op_sel_hi:[0,1,1]
	v_cvt_pk_f32_fp8_sdwa v[166:167], v60 src0_sel:WORD_1
	v_pk_fma_f32 v[30:31], v[116:117], v[224:225], v[30:31] op_sel_hi:[0,1,1]
	v_cvt_pk_f32_fp8_sdwa v[178:179], v56 src0_sel:WORD_1
	ds_write_b128 v246, v[26:29] offset:16
	v_pk_fma_f32 v[30:31], v[144:145], v[238:239], v[30:31] op_sel_hi:[0,1,1]
	v_cvt_pk_f32_fp8_sdwa v[190:191], v48 src0_sel:WORD_1
	v_lshlrev_b32_e32 v28, 16, v6
	v_and_b32_e32 v29, 0xffff0000, v6
	v_lshlrev_b32_e32 v26, 16, v2
	v_and_b32_e32 v27, 0xffff0000, v2
	v_pk_add_f32 v[28:29], v[30:31], v[28:29]
	v_cvt_pk_f32_fp8_sdwa v[202:203], v52 src0_sel:WORD_1
	v_pk_fma_f32 v[26:27], v[18:19], v[28:29], v[26:27]
	v_pk_fma_f32 v[28:29], v[118:119], v[154:155], 0 op_sel_hi:[0,1,0]
	v_cvt_pk_f32_fp8_sdwa v[214:215], v44 src0_sel:WORD_1
; __device__ void phase6(const Params& p) {
;     ...
;         const unsigned xw[8] = {xa.x, xa.y, xa.z, xa.w, xb.x, xb.y, xb.z, xb.w}, sw[8] = {sa.x, sa.y, sa.z, sa.w, sb.x, sb.y, sb.z, sb.w};
; #pragma unroll
;         for (int q = 0; q < 4; ++q) {
;             const int col = lane * 16 + q * 4;
;             const float4 g2 = g2v[q];
;             float4 r;
;             r.x = __uint_as_float(xw[q * 2] << 16) + g2.x * (sacc[q * 4 + 0] + __uint_as_float(sw[q * 2] << 16));
;             r.y = __uint_as_float(xw[q * 2] & 0xffff0000u) + g2.y * (sacc[q * 4 + 1] + __uint_as_float(sw[q * 2] & 0xffff0000u));
;             r.z = __uint_as_float(xw[q * 2 + 1] << 16) + g2.z * (sacc[q * 4 + 2] + __uint_as_float(sw[q * 2 + 1] << 16));
;             r.w = __uint_as_float(xw[q * 2 + 1] & 0xffff0000u) + g2.w * (sacc[q * 4 + 3] + __uint_as_float(sw[q * 2 + 1] & 0xffff0000u));
;             *(float4*)(p.out + (size_t)R * D + col) = r;
;         }
;         if (!more) break;
;         R = Rn;
	v_pk_fma_f32 v[28:29], v[138:139], v[166:167], v[28:29] op_sel_hi:[0,1,1]
	v_cvt_pk_f32_fp8_sdwa v[226:227], v40 src0_sel:WORD_1
	v_pk_fma_f32 v[28:29], v[120:121], v[178:179], v[28:29] op_sel_hi:[0,1,1]
	v_pk_fma_f32 v[28:29], v[140:141], v[190:191], v[28:29] op_sel_hi:[0,1,1]
	v_pk_fma_f32 v[28:29], v[114:115], v[202:203], v[28:29] op_sel_hi:[0,1,1]
	v_pk_fma_f32 v[28:29], v[142:143], v[214:215], v[28:29] op_sel_hi:[0,1,1]
	v_cvt_pk_f32_fp8_e32 v[156:157], v65
	v_pk_fma_f32 v[28:29], v[116:117], v[226:227], v[28:29] op_sel_hi:[0,1,1]
	v_cvt_pk_f32_fp8_e32 v[168:169], v61
	v_lshlrev_b32_e32 v6, 16, v7
	v_and_b32_e32 v7, 0xffff0000, v7
	v_pk_fma_f32 v[28:29], v[144:145], v[240:241], v[28:29] op_sel_hi:[0,1,1]
	v_cvt_pk_f32_fp8_e32 v[180:181], v57
	v_lshlrev_b32_e32 v2, 16, v3
	v_and_b32_e32 v3, 0xffff0000, v3
	v_pk_add_f32 v[6:7], v[28:29], v[6:7]
	v_cvt_pk_f32_fp8_e32 v[192:193], v49
	v_pk_fma_f32 v[28:29], v[20:21], v[6:7], v[2:3]
	v_cvt_pk_f32_fp8_e32 v[204:205], v53
	ds_write_b128 v246, v[26:29] offset:32
	v_cvt_pk_f32_fp8_e32 v[216:217], v45
	v_cvt_pk_f32_fp8_e32 v[228:229], v41
	v_pk_fma_f32 v[26:27], v[118:119], v[156:157], 0 op_sel_hi:[0,1,0]
	v_pk_fma_f32 v[26:27], v[138:139], v[168:169], v[26:27] op_sel_hi:[0,1,1]
	v_pk_fma_f32 v[26:27], v[120:121], v[180:181], v[26:27] op_sel_hi:[0,1,1]
	v_pk_fma_f32 v[26:27], v[140:141], v[192:193], v[26:27] op_sel_hi:[0,1,1]
	v_pk_fma_f32 v[26:27], v[114:115], v[204:205], v[26:27] op_sel_hi:[0,1,1]
	v_cvt_pk_f32_fp8_sdwa v[64:65], v65 src0_sel:WORD_1
	v_pk_fma_f32 v[26:27], v[142:143], v[216:217], v[26:27] op_sel_hi:[0,1,1]
	v_cvt_pk_f32_fp8_sdwa v[60:61], v61 src0_sel:WORD_1
	v_pk_fma_f32 v[26:27], v[116:117], v[228:229], v[26:27] op_sel_hi:[0,1,1]
	v_cvt_pk_f32_fp8_sdwa v[56:57], v57 src0_sel:WORD_1
	v_lshlrev_b32_e32 v6, 16, v8
	v_and_b32_e32 v7, 0xffff0000, v8
	v_pk_fma_f32 v[26:27], v[144:145], v[242:243], v[26:27] op_sel_hi:[0,1,1]
	v_cvt_pk_f32_fp8_sdwa v[48:49], v49 src0_sel:WORD_1
	v_lshlrev_b32_e32 v2, 16, v4
	v_and_b32_e32 v3, 0xffff0000, v4
	v_pk_add_f32 v[6:7], v[26:27], v[6:7]
	v_cvt_pk_f32_fp8_sdwa v[52:53], v53 src0_sel:WORD_1
	v_pk_fma_f32 v[2:3], v[22:23], v[6:7], v[2:3]
	v_pk_fma_f32 v[6:7], v[118:119], v[64:65], 0 op_sel_hi:[0,1,0]
	v_cvt_pk_f32_fp8_sdwa v[44:45], v45 src0_sel:WORD_1
	v_pk_fma_f32 v[6:7], v[138:139], v[60:61], v[6:7] op_sel_hi:[0,1,1]
	v_cvt_pk_f32_fp8_sdwa v[40:41], v41 src0_sel:WORD_1
	v_pk_fma_f32 v[6:7], v[120:121], v[56:57], v[6:7] op_sel_hi:[0,1,1]
	v_pk_fma_f32 v[6:7], v[140:141], v[48:49], v[6:7] op_sel_hi:[0,1,1]
	v_pk_fma_f32 v[6:7], v[114:115], v[52:53], v[6:7] op_sel_hi:[0,1,1]
	v_pk_fma_f32 v[6:7], v[142:143], v[44:45], v[6:7] op_sel_hi:[0,1,1]
	v_pk_fma_f32 v[6:7], v[116:117], v[40:41], v[6:7] op_sel_hi:[0,1,1]
	v_lshlrev_b32_e32 v8, 16, v9
	v_and_b32_e32 v9, 0xffff0000, v9
	v_pk_fma_f32 v[6:7], v[144:145], v[244:245], v[6:7] op_sel_hi:[0,1,1]
	v_lshlrev_b32_e32 v4, 16, v5
	v_and_b32_e32 v5, 0xffff0000, v5
	v_pk_add_f32 v[6:7], v[6:7], v[8:9]
	s_and_b64 s[0:1], exec, s[0:1]
	v_pk_fma_f32 v[4:5], v[24:25], v[6:7], v[4:5]
	s_or_b64 s[10:11], s[0:1], s[10:11]
	ds_write_b128 v246, v[2:5] offset:48
	s_waitcnt lgkmcnt(0)
	ds_read_b128 v[2:5], v247
	ds_read_b128 v[6:9], v247 offset:128
	ds_read_b128 v[26:29], v247 offset:256
	ds_read_b128 v[30:33], v247 offset:384
	v_lshl_add_u64 v[254:255], v[0:1], 0, v[252:253]
	s_waitcnt lgkmcnt(0)
	global_store_dwordx4 v[254:255], v[2:5], off
	global_store_dwordx4 v[254:255], v[6:9], off offset:128
	global_store_dwordx4 v[254:255], v[26:29], off offset:256
	global_store_dwordx4 v[254:255], v[30:33], off offset:384
	v_lshl_add_u64 v[0:1], v[0:1], 0, s[2:3]
	v_lshl_add_u64 v[132:133], v[132:133], 0, s[4:5]
	v_lshl_add_u64 v[134:135], v[134:135], 0, s[6:7]
	v_lshl_add_u64 v[136:137], v[136:137], 0, s[8:9]
	v_mov_b32_e32 v138, v141
	v_mov_b64_e32 v[114:115], v[126:127]
	v_mov_b64_e32 v[116:117], v[128:129]
	v_mov_b64_e32 v[118:119], v[122:123]
	v_mov_b64_e32 v[120:121], v[124:125]
	v_mov_b64_e32 v[62:63], v[66:67]
	v_mov_b64_e32 v[64:65], v[68:69]
	v_mov_b64_e32 v[58:59], v[70:71]
	v_mov_b64_e32 v[60:61], v[72:73]
	v_mov_b64_e32 v[54:55], v[74:75]
	v_mov_b64_e32 v[56:57], v[76:77]
	v_mov_b64_e32 v[46:47], v[78:79]
	v_mov_b64_e32 v[48:49], v[80:81]
	v_mov_b64_e32 v[50:51], v[82:83]
	v_mov_b64_e32 v[52:53], v[84:85]
	v_mov_b64_e32 v[42:43], v[86:87]
	v_mov_b64_e32 v[44:45], v[88:89]
	v_mov_b64_e32 v[38:39], v[90:91]
	v_mov_b64_e32 v[40:41], v[92:93]
	v_mov_b64_e32 v[34:35], v[94:95]
	v_mov_b64_e32 v[36:37], v[96:97]
	v_mov_b64_e32 v[6:7], v[110:111]
	v_mov_b64_e32 v[8:9], v[112:113]
	v_mov_b64_e32 v[30:31], v[106:107]
	v_mov_b64_e32 v[32:33], v[108:109]
	v_mov_b64_e32 v[2:3], v[102:103]
	v_mov_b64_e32 v[4:5], v[104:105]
	v_mov_b64_e32 v[26:27], v[98:99]
	v_mov_b64_e32 v[28:29], v[100:101]
	s_andn2_b64 exec, exec, s[10:11]
	s_cbranch_execz .LBB0_1296
